# gate/up routed loop: A fragments of the next step requested at step start (own registers, before the B loads), even-step waits made steady-state exact; extra-row instance: A wait moved after the barri
# speedup vs baseline: 1.0144x; 1.0063x over previous
.LBB0_1306:
	s_add_i32 s25, s2, 1
	s_cmp_lg_u32 s2, 2
	s_cselect_b32 s26, s25, 0
	s_mul_i32 s25, s26, 0x4800
	s_add_i32 s56, s25, 0
	s_add_i32 s25, s39, 3
	s_cmp_lt_u32 s39, 61
	s_cselect_b32 s25, s25, 0
	s_lshr_b32 s42, s25, 4
	s_add_i32 s42, s42, s66
	s_and_b32 s42, s42, 3
	s_add_i32 s42, s42, s27
	s_lshl_b32 s25, s25, 16
	s_lshl_b32 s42, s42, 8
	s_and_b32 s25, s25, 0xf0000
	v_add_u32_e32 v0, s56, v239
	s_cmp_lg_u32 s39, 0
	s_cbranch_scc1 .Lgx_es
	s_waitcnt vmcnt(4)
.Lgx_es:
	s_waitcnt vmcnt(10)
	v_cvt_pk_bf16_f32 v2, v160, v164
	v_cvt_pk_bf16_f32 v3, v168, v172
	s_or_b32 s25, s42, s25
	s_waitcnt lgkmcnt(0)
	s_barrier
	ds_write2_b32 v0, v2, v3 offset1:8
	v_cvt_pk_bf16_f32 v2, v161, v165
	v_cvt_pk_bf16_f32 v3, v169, v173
	v_add_u32_e32 v4, 0x400, v0
	s_add_u32 s42, s67, s25
	ds_write2_b32 v4, v2, v3 offset0:32 offset1:40
	v_cvt_pk_bf16_f32 v2, v162, v166
	v_cvt_pk_bf16_f32 v3, v170, v174
	v_add_u32_e32 v4, 0x800, v0
	s_addc_u32 s43, s38, 0
	ds_write2_b32 v4, v2, v3 offset0:64 offset1:72
	v_cvt_pk_bf16_f32 v2, v163, v167
	v_cvt_pk_bf16_f32 v3, v171, v175
	v_add_u32_e32 v0, 0xc00, v0
	s_add_u32 s46, s42, 0x4000
	ds_write2_b32 v0, v2, v3 offset0:96 offset1:104
	s_addc_u32 s47, s43, 0
	v_mov_b32_e32 v0, v238
	global_load_dwordx4 v[160:163], v0, s[42:43] nt
	global_load_dwordx4 v[164:167], v0, s[42:43] offset:1024 nt
	global_load_dwordx4 v[168:171], v0, s[46:47] nt
	global_load_dwordx4 v[172:175], v0, s[46:47] offset:1024 nt
	s_add_i32 s25, s49, 0xffffff80
	s_and_b32 s25, s25, 0x380
	s_or_b32 s25, s25, 64
	s_add_u32 s46, s25, s54
	v_cndmask_b32_e64 v0, 0, 1, s[0:1]
	s_addc_u32 s47, 0, s55
	s_mul_i32 s90, s2, 0x4800
	v_cmp_ne_u32_e64 s[42:43], 1, v0
	s_andn2_b64 vcc, exec, s[0:1]
	s_cbranch_vccnz .LBB0_1308
	s_waitcnt vmcnt(8)
	v_cvt_pk_f32_fp8_e32 v[6:7], v212
	v_cvt_pk_f32_fp8_sdwa v[8:9], v212 src0_sel:WORD_1
	v_cvt_pk_f32_fp8_e32 v[10:11], v213
	v_cvt_pk_f32_fp8_sdwa v[12:13], v213 src0_sel:WORD_1
	v_add_u32_e32 v0, s90, v245
	ds_read_b128 v[2:5], v0
	v_cvt_pk_bf16_f32 v6, v6, v7
	v_cvt_pk_bf16_f32 v7, v8, v9
	v_cvt_pk_bf16_f32 v8, v10, v11
	v_cvt_pk_bf16_f32 v9, v12, v13
	ds_read_b128 v[10:13], v0 offset:4608
	ds_read_b128 v[248:251], v0 offset:9216
	ds_read_b128 v[216:219], v0 offset:13824
	s_waitcnt lgkmcnt(3)
	v_mfma_f32_32x32x16_bf16 v[144:159], v[2:5], v[6:9], v[144:159]
	s_waitcnt vmcnt(6)
	v_cvt_pk_f32_fp8_e32 v[14:15], v209
	s_waitcnt lgkmcnt(2)
	v_mfma_f32_32x32x16_bf16 v[112:127], v[10:13], v[6:9], v[112:127]
	s_waitcnt lgkmcnt(1)
	v_mfma_f32_32x32x16_bf16 v[128:143], v[248:251], v[6:9], v[128:143]
	s_waitcnt lgkmcnt(0)
	v_mfma_f32_32x32x16_bf16 v[96:111], v[216:219], v[6:9], v[96:111]
	v_cvt_pk_f32_fp8_e32 v[6:7], v208
	v_cvt_pk_f32_fp8_sdwa v[8:9], v208 src0_sel:WORD_1
	v_cvt_pk_f32_fp8_sdwa v[208:209], v209 src0_sel:WORD_1
	v_cvt_pk_bf16_f32 v6, v6, v7
	v_cvt_pk_bf16_f32 v7, v8, v9
	v_cvt_pk_bf16_f32 v8, v14, v15
	v_cvt_pk_bf16_f32 v9, v208, v209
	v_cvt_pk_f32_fp8_e32 v[14:15], v211
	v_cvt_pk_f32_fp8_sdwa v[208:209], v211 src0_sel:WORD_1
	v_mfma_f32_32x32x16_bf16 v[80:95], v[2:5], v[6:9], v[80:95]
	ds_read_b128 v[2:5], v0 offset:16
	v_mfma_f32_32x32x16_bf16 v[48:63], v[10:13], v[6:9], v[48:63]
	v_cvt_pk_f32_fp8_e32 v[10:11], v215
	v_cvt_pk_f32_fp8_sdwa v[12:13], v215 src0_sel:WORD_1
	v_mfma_f32_32x32x16_bf16 v[64:79], v[248:251], v[6:9], v[64:79]
	v_mfma_f32_32x32x16_bf16 v[32:47], v[216:219], v[6:9], v[32:47]
	v_cvt_pk_f32_fp8_e32 v[6:7], v214
	v_cvt_pk_f32_fp8_sdwa v[8:9], v214 src0_sel:WORD_1
	ds_read_b128 v[212:215], v0 offset:9232
	ds_read_b128 v[216:219], v0 offset:13840
	v_cvt_pk_bf16_f32 v6, v6, v7
	v_cvt_pk_bf16_f32 v7, v8, v9
	v_cvt_pk_bf16_f32 v8, v10, v11
	v_cvt_pk_bf16_f32 v9, v12, v13
	ds_read_b128 v[10:13], v0 offset:4624
	s_waitcnt lgkmcnt(3)
	v_mfma_f32_32x32x16_bf16 v[144:159], v[2:5], v[6:9], v[144:159]
	s_waitcnt lgkmcnt(0)
	v_mfma_f32_32x32x16_bf16 v[112:127], v[10:13], v[6:9], v[112:127]
	v_mfma_f32_32x32x16_bf16 v[128:143], v[212:215], v[6:9], v[128:143]
	v_mfma_f32_32x32x16_bf16 v[96:111], v[216:219], v[6:9], v[96:111]
	v_cvt_pk_f32_fp8_e32 v[6:7], v210
	v_cvt_pk_f32_fp8_sdwa v[8:9], v210 src0_sel:WORD_1
	v_cvt_pk_bf16_f32 v6, v6, v7
	v_cvt_pk_bf16_f32 v7, v8, v9
	v_cvt_pk_bf16_f32 v8, v14, v15
	v_cvt_pk_bf16_f32 v9, v208, v209
	ds_read_b128 v[208:211], v0 offset:9248
	v_cvt_pk_f32_fp8_e32 v[14:15], v193
	v_mfma_f32_32x32x16_bf16 v[80:95], v[2:5], v[6:9], v[80:95]
	ds_read_b128 v[2:5], v0 offset:32
	v_mfma_f32_32x32x16_bf16 v[48:63], v[10:13], v[6:9], v[48:63]
	v_cvt_pk_f32_fp8_e32 v[10:11], v205
	v_cvt_pk_f32_fp8_sdwa v[12:13], v205 src0_sel:WORD_1
	v_mfma_f32_32x32x16_bf16 v[64:79], v[212:215], v[6:9], v[64:79]
	ds_read_b128 v[212:215], v0 offset:13856
	v_mfma_f32_32x32x16_bf16 v[32:47], v[216:219], v[6:9], v[32:47]
	v_cvt_pk_f32_fp8_e32 v[6:7], v204
	v_cvt_pk_f32_fp8_sdwa v[8:9], v204 src0_sel:WORD_1
	v_cvt_pk_bf16_f32 v6, v6, v7
	v_cvt_pk_bf16_f32 v7, v8, v9
	v_cvt_pk_bf16_f32 v8, v10, v11
	v_cvt_pk_bf16_f32 v9, v12, v13
	ds_read_b128 v[10:13], v0 offset:4640
	s_waitcnt lgkmcnt(2)
	v_mfma_f32_32x32x16_bf16 v[144:159], v[2:5], v[6:9], v[144:159]
	s_waitcnt lgkmcnt(0)
	v_mfma_f32_32x32x16_bf16 v[112:127], v[10:13], v[6:9], v[112:127]
	v_mfma_f32_32x32x16_bf16 v[128:143], v[208:211], v[6:9], v[128:143]
	v_mfma_f32_32x32x16_bf16 v[96:111], v[212:215], v[6:9], v[96:111]
	v_cvt_pk_f32_fp8_e32 v[6:7], v192
	v_cvt_pk_f32_fp8_sdwa v[8:9], v192 src0_sel:WORD_1
	v_cvt_pk_f32_fp8_sdwa v[192:193], v193 src0_sel:WORD_1
	v_cvt_pk_bf16_f32 v6, v6, v7
	v_cvt_pk_bf16_f32 v7, v8, v9
	v_cvt_pk_bf16_f32 v8, v14, v15
	v_cvt_pk_bf16_f32 v9, v192, v193
	v_cvt_pk_f32_fp8_e32 v[14:15], v195
	v_cvt_pk_f32_fp8_sdwa v[192:193], v195 src0_sel:WORD_1
	v_mfma_f32_32x32x16_bf16 v[80:95], v[2:5], v[6:9], v[80:95]
	ds_read_b128 v[2:5], v0 offset:48
	v_mfma_f32_32x32x16_bf16 v[48:63], v[10:13], v[6:9], v[48:63]
	v_cvt_pk_f32_fp8_e32 v[10:11], v207
	v_cvt_pk_f32_fp8_sdwa v[12:13], v207 src0_sel:WORD_1
	v_mfma_f32_32x32x16_bf16 v[64:79], v[208:211], v[6:9], v[64:79]
	ds_read_b128 v[208:211], v0 offset:13872
	v_mfma_f32_32x32x16_bf16 v[32:47], v[212:215], v[6:9], v[32:47]
	v_cvt_pk_f32_fp8_e32 v[6:7], v206
	v_cvt_pk_f32_fp8_sdwa v[8:9], v206 src0_sel:WORD_1
	ds_read_b128 v[204:207], v0 offset:9264
	v_cvt_pk_bf16_f32 v6, v6, v7
	v_cvt_pk_bf16_f32 v7, v8, v9
	v_cvt_pk_bf16_f32 v8, v10, v11
	v_cvt_pk_bf16_f32 v9, v12, v13
	ds_read_b128 v[10:13], v0 offset:4656
	s_waitcnt lgkmcnt(3)
	v_mfma_f32_32x32x16_bf16 v[144:159], v[2:5], v[6:9], v[144:159]
	s_waitcnt lgkmcnt(0)
	v_mfma_f32_32x32x16_bf16 v[112:127], v[10:13], v[6:9], v[112:127]
	v_mfma_f32_32x32x16_bf16 v[128:143], v[204:207], v[6:9], v[128:143]
	v_mfma_f32_32x32x16_bf16 v[96:111], v[208:211], v[6:9], v[96:111]
	v_cvt_pk_f32_fp8_e32 v[6:7], v194
	v_cvt_pk_f32_fp8_sdwa v[8:9], v194 src0_sel:WORD_1
	v_cvt_pk_bf16_f32 v6, v6, v7
	v_cvt_pk_bf16_f32 v7, v8, v9
	v_cvt_pk_bf16_f32 v8, v14, v15
	v_cvt_pk_bf16_f32 v9, v192, v193
	s_nop 1
	v_mfma_f32_32x32x16_bf16 v[80:95], v[2:5], v[6:9], v[80:95]
	v_mfma_f32_32x32x16_bf16 v[48:63], v[10:13], v[6:9], v[48:63]
	v_mfma_f32_32x32x16_bf16 v[64:79], v[204:207], v[6:9], v[64:79]
	v_mfma_f32_32x32x16_bf16 v[32:47], v[208:211], v[6:9], v[32:47]

.LBB0_1324:
	s_sub_i32 s98, s2, 64
	s_add_i32 s99, s49, -1
	s_and_b32 s98, s98, 0x3c0
	s_cmp_lt_u32 s99, s40
	s_cselect_b32 s98, s98, 0
	s_add_u32 s98, s98, s54
	s_addc_u32 s99, 0, s55
	global_load_dwordx4 v[206:209], v194, s[98:99] offset:16
	global_load_dwordx4 v[210:213], v194, s[98:99]
	global_load_dwordx4 v[214:217], v195, s[98:99] offset:16
	global_load_dwordx4 v[248:251], v195, s[98:99]
	s_add_i32 s0, s29, 1
	s_cmp_lg_u32 s29, 2
	s_cselect_b32 s39, s0, 0
	s_mul_i32 s0, s39, 0x4800
	s_add_i32 s26, s0, 0
	s_add_i32 s0, s49, 1
	s_cmp_lt_u32 s0, s40
	s_cselect_b32 s0, s0, 0
	s_lshr_b32 s1, s0, 4
	s_add_i32 s1, s1, s76
	s_and_b32 s1, s1, s77
	s_add_i32 s1, s1, s27
	s_lshl_b32 s0, s0, 14
	s_lshl_b32 s1, s1, 6
	s_and_b32 s0, s0, 0x3c000
	s_add_i32 s56, s1, s0
	v_add_u32_e32 v0, s26, v193
	s_cmp_lg_u32 s49, 2
	s_cbranch_scc1 .Lgu_es
	s_waitcnt vmcnt(8)
.Lgu_es:
	s_waitcnt vmcnt(12)
	v_cvt_pk_bf16_f32 v2, v144, v148
	v_cvt_pk_bf16_f32 v3, v152, v156
	s_lshl_b64 s[0:1], s[56:57], 2
	s_waitcnt lgkmcnt(0)
	s_barrier
	ds_write2_b32 v0, v2, v3 offset1:8
	v_cvt_pk_bf16_f32 v2, v145, v149
	v_cvt_pk_bf16_f32 v3, v153, v157
	v_add_u32_e32 v4, 0x400, v0
	s_add_u32 s0, s11, s0
	ds_write2_b32 v4, v2, v3 offset0:32 offset1:40
	v_cvt_pk_bf16_f32 v2, v146, v150
	v_cvt_pk_bf16_f32 v3, v154, v158
	v_add_u32_e32 v4, 0x800, v0
	s_addc_u32 s1, s79, s1
	ds_write2_b32 v4, v2, v3 offset0:64 offset1:72
	v_cvt_pk_bf16_f32 v2, v147, v151
	v_cvt_pk_bf16_f32 v3, v155, v159
	v_add_u32_e32 v0, 0xc00, v0
	s_add_u32 s46, s0, 0x4000
	ds_write2_b32 v0, v2, v3 offset0:96 offset1:104
	s_addc_u32 s47, s1, 0
	v_mov_b32_e32 v0, v192
	global_load_dwordx4 v[144:147], v0, s[0:1] nt
	global_load_dwordx4 v[148:151], v0, s[0:1] offset:1024 nt
	global_load_dwordx4 v[152:155], v0, s[46:47] nt
	global_load_dwordx4 v[156:159], v0, s[46:47] offset:1024 nt
	s_sub_i32 s1, s2, 64
	s_add_i32 s0, s49, -1
	s_and_b32 s1, s1, 0x3c0
	s_cmp_lt_u32 s0, s40
	s_cselect_b32 s0, s1, 0
	s_add_u32 s46, s0, s54
	v_cndmask_b32_e64 v0, 0, 1, s[42:43]
	s_addc_u32 s47, 0, s55
	v_cmp_ne_u32_e64 s[0:1], 1, v0
	s_andn2_b64 vcc, exec, s[42:43]
	s_cbranch_vccnz .LBB0_1326
	s_waitcnt vmcnt(14)
	v_cvt_pk_f32_fp8_e32 v[6:7], v188
	v_cvt_pk_f32_fp8_sdwa v[8:9], v188 src0_sel:WORD_1
	v_cvt_pk_f32_fp8_e32 v[10:11], v189
	v_cvt_pk_f32_fp8_sdwa v[12:13], v189 src0_sel:WORD_1
	s_mul_i32 s25, s29, 0x4800
	v_add_u32_e32 v0, s25, v197
	ds_read_b128 v[2:5], v0
	v_cvt_pk_bf16_f32 v6, v6, v7
	v_cvt_pk_bf16_f32 v7, v8, v9
	v_cvt_pk_bf16_f32 v8, v10, v11
	v_cvt_pk_bf16_f32 v9, v12, v13
	ds_read_b128 v[10:13], v0 offset:4608
	ds_read_b128 v[198:201], v0 offset:9216
	ds_read_b128 v[202:205], v0 offset:13824
	s_waitcnt lgkmcnt(3)
	v_mfma_f32_32x32x16_bf16 v[128:143], v[2:5], v[6:9], v[128:143]
	s_waitcnt vmcnt(12)
	v_cvt_pk_f32_fp8_e32 v[14:15], v185
	s_waitcnt lgkmcnt(2)
	v_mfma_f32_32x32x16_bf16 v[96:111], v[10:13], v[6:9], v[96:111]
	s_waitcnt lgkmcnt(1)
	v_mfma_f32_32x32x16_bf16 v[112:127], v[198:201], v[6:9], v[112:127]
	s_waitcnt lgkmcnt(0)
	v_mfma_f32_32x32x16_bf16 v[80:95], v[202:205], v[6:9], v[80:95]
	v_cvt_pk_f32_fp8_e32 v[6:7], v184
	v_cvt_pk_f32_fp8_sdwa v[8:9], v184 src0_sel:WORD_1
	v_cvt_pk_f32_fp8_sdwa v[184:185], v185 src0_sel:WORD_1
	v_cvt_pk_bf16_f32 v6, v6, v7
	v_cvt_pk_bf16_f32 v7, v8, v9
	v_cvt_pk_bf16_f32 v8, v14, v15
	v_cvt_pk_bf16_f32 v9, v184, v185
	v_cvt_pk_f32_fp8_e32 v[14:15], v187
	v_cvt_pk_f32_fp8_sdwa v[184:185], v187 src0_sel:WORD_1
	v_mfma_f32_32x32x16_bf16 v[64:79], v[2:5], v[6:9], v[64:79]
	ds_read_b128 v[2:5], v0 offset:16
	v_mfma_f32_32x32x16_bf16 v[32:47], v[10:13], v[6:9], v[32:47]
	v_cvt_pk_f32_fp8_e32 v[10:11], v191
	v_cvt_pk_f32_fp8_sdwa v[12:13], v191 src0_sel:WORD_1
	v_mfma_f32_32x32x16_bf16 v[48:63], v[198:201], v[6:9], v[48:63]
	ds_read_b128 v[198:201], v0 offset:13840
	v_mfma_f32_32x32x16_bf16 v[16:31], v[202:205], v[6:9], v[16:31]
	v_cvt_pk_f32_fp8_e32 v[6:7], v190
	v_cvt_pk_f32_fp8_sdwa v[8:9], v190 src0_sel:WORD_1
	ds_read_b128 v[188:191], v0 offset:9232
	v_cvt_pk_bf16_f32 v6, v6, v7
	v_cvt_pk_bf16_f32 v7, v8, v9
	v_cvt_pk_bf16_f32 v8, v10, v11
	v_cvt_pk_bf16_f32 v9, v12, v13
	ds_read_b128 v[10:13], v0 offset:4624
	s_waitcnt lgkmcnt(3)
	v_mfma_f32_32x32x16_bf16 v[128:143], v[2:5], v[6:9], v[128:143]
	s_waitcnt lgkmcnt(0)
	v_mfma_f32_32x32x16_bf16 v[96:111], v[10:13], v[6:9], v[96:111]
	v_mfma_f32_32x32x16_bf16 v[112:127], v[188:191], v[6:9], v[112:127]
	v_mfma_f32_32x32x16_bf16 v[80:95], v[198:201], v[6:9], v[80:95]
	v_cvt_pk_f32_fp8_e32 v[6:7], v186
	v_cvt_pk_f32_fp8_sdwa v[8:9], v186 src0_sel:WORD_1
	v_cvt_pk_bf16_f32 v6, v6, v7
	v_cvt_pk_bf16_f32 v7, v8, v9
	v_cvt_pk_bf16_f32 v8, v14, v15
	v_cvt_pk_bf16_f32 v9, v184, v185
	ds_read_b128 v[184:187], v0 offset:9248
	v_cvt_pk_f32_fp8_e32 v[14:15], v177
	v_mfma_f32_32x32x16_bf16 v[64:79], v[2:5], v[6:9], v[64:79]
	ds_read_b128 v[2:5], v0 offset:32
	v_mfma_f32_32x32x16_bf16 v[32:47], v[10:13], v[6:9], v[32:47]
	v_cvt_pk_f32_fp8_e32 v[10:11], v181
	v_cvt_pk_f32_fp8_sdwa v[12:13], v181 src0_sel:WORD_1
	v_mfma_f32_32x32x16_bf16 v[48:63], v[188:191], v[6:9], v[48:63]
	ds_read_b128 v[188:191], v0 offset:13856
	v_mfma_f32_32x32x16_bf16 v[16:31], v[198:201], v[6:9], v[16:31]
	v_cvt_pk_f32_fp8_e32 v[6:7], v180
	v_cvt_pk_f32_fp8_sdwa v[8:9], v180 src0_sel:WORD_1
	v_cvt_pk_bf16_f32 v6, v6, v7
	v_cvt_pk_bf16_f32 v7, v8, v9
	v_cvt_pk_bf16_f32 v8, v10, v11
	v_cvt_pk_bf16_f32 v9, v12, v13
	ds_read_b128 v[10:13], v0 offset:4640
	s_waitcnt lgkmcnt(2)
	v_mfma_f32_32x32x16_bf16 v[128:143], v[2:5], v[6:9], v[128:143]
	s_waitcnt lgkmcnt(0)
	v_mfma_f32_32x32x16_bf16 v[96:111], v[10:13], v[6:9], v[96:111]
	v_mfma_f32_32x32x16_bf16 v[112:127], v[184:187], v[6:9], v[112:127]
	v_mfma_f32_32x32x16_bf16 v[80:95], v[188:191], v[6:9], v[80:95]
	v_cvt_pk_f32_fp8_e32 v[6:7], v176
	v_cvt_pk_f32_fp8_sdwa v[8:9], v176 src0_sel:WORD_1
	v_cvt_pk_f32_fp8_sdwa v[176:177], v177 src0_sel:WORD_1
	v_cvt_pk_bf16_f32 v6, v6, v7
	v_cvt_pk_bf16_f32 v7, v8, v9
	v_cvt_pk_bf16_f32 v8, v14, v15
	v_cvt_pk_bf16_f32 v9, v176, v177
	v_cvt_pk_f32_fp8_e32 v[14:15], v179
	v_cvt_pk_f32_fp8_sdwa v[176:177], v179 src0_sel:WORD_1
	v_mfma_f32_32x32x16_bf16 v[64:79], v[2:5], v[6:9], v[64:79]
	ds_read_b128 v[2:5], v0 offset:48
	v_mfma_f32_32x32x16_bf16 v[32:47], v[10:13], v[6:9], v[32:47]
	v_cvt_pk_f32_fp8_e32 v[10:11], v183
	v_cvt_pk_f32_fp8_sdwa v[12:13], v183 src0_sel:WORD_1
	v_mfma_f32_32x32x16_bf16 v[48:63], v[184:187], v[6:9], v[48:63]
	ds_read_b128 v[184:187], v0 offset:13872
	v_mfma_f32_32x32x16_bf16 v[16:31], v[188:191], v[6:9], v[16:31]
	v_cvt_pk_f32_fp8_e32 v[6:7], v182
	v_cvt_pk_f32_fp8_sdwa v[8:9], v182 src0_sel:WORD_1
	ds_read_b128 v[180:183], v0 offset:9264
	v_cvt_pk_bf16_f32 v6, v6, v7
	v_cvt_pk_bf16_f32 v7, v8, v9
	v_cvt_pk_bf16_f32 v8, v10, v11
	v_cvt_pk_bf16_f32 v9, v12, v13
	ds_read_b128 v[10:13], v0 offset:4656
	s_waitcnt lgkmcnt(3)
	v_mfma_f32_32x32x16_bf16 v[128:143], v[2:5], v[6:9], v[128:143]
	s_waitcnt lgkmcnt(0)
	v_mfma_f32_32x32x16_bf16 v[96:111], v[10:13], v[6:9], v[96:111]
	v_mfma_f32_32x32x16_bf16 v[112:127], v[180:183], v[6:9], v[112:127]
	v_mfma_f32_32x32x16_bf16 v[80:95], v[184:187], v[6:9], v[80:95]
	v_cvt_pk_f32_fp8_e32 v[6:7], v178
	v_cvt_pk_f32_fp8_sdwa v[8:9], v178 src0_sel:WORD_1
	v_cvt_pk_bf16_f32 v6, v6, v7
	v_cvt_pk_bf16_f32 v7, v8, v9
	v_cvt_pk_bf16_f32 v8, v14, v15
	v_cvt_pk_bf16_f32 v9, v176, v177
	s_nop 1
	v_mfma_f32_32x32x16_bf16 v[64:79], v[2:5], v[6:9], v[64:79]
	v_mfma_f32_32x32x16_bf16 v[32:47], v[10:13], v[6:9], v[32:47]
	v_mfma_f32_32x32x16_bf16 v[48:63], v[180:183], v[6:9], v[48:63]
	v_mfma_f32_32x32x16_bf16 v[16:31], v[184:187], v[6:9], v[16:31]
.LBB0_1326:
	s_and_b32 s98, s2, 0x380
	s_cmp_lt_u32 s49, s40
	s_cselect_b32 s98, s98, 0
	s_add_u32 s98, s98, s54
	s_addc_u32 s99, 0, s55
	global_load_dwordx4 v[180:183], v194, s[98:99] offset:16
	global_load_dwordx4 v[188:191], v194, s[98:99]
	global_load_dwordx4 v[176:179], v195, s[98:99] offset:16
	global_load_dwordx4 v[184:187], v195, s[98:99]
	s_add_i32 s25, s39, 1
	s_cmp_lg_u32 s39, 2
	s_cselect_b32 s29, s25, 0
	s_add_i32 s39, s49, 2
	s_mul_i32 s25, s29, 0x4800
	s_cmp_lt_u32 s39, s40
	v_add_u32_e32 v0, s25, v196
	s_cselect_b32 s25, s39, 0
	s_lshr_b32 s46, s25, 4
	s_add_i32 s46, s46, s76
	s_and_b32 s46, s46, s77
	s_add_i32 s46, s46, s27
	s_lshl_b32 s25, s25, 14
	s_lshl_b32 s46, s46, 6
	s_and_b32 s25, s25, 0x38000
	s_add_i32 s56, s46, s25
	s_waitcnt vmcnt(12)
	v_cvt_pk_bf16_f32 v14, v160, v164
	v_cvt_pk_bf16_f32 v15, v168, v172
	s_lshl_b64 s[46:47], s[56:57], 2
	s_waitcnt lgkmcnt(0)
	s_barrier
	ds_write2_b32 v0, v14, v15 offset1:8
	v_cvt_pk_bf16_f32 v14, v161, v165
	v_cvt_pk_bf16_f32 v15, v169, v173
	v_add_u32_e32 v160, 0x400, v0
	s_add_u32 s46, s11, s46
	ds_write2_b32 v160, v14, v15 offset0:32 offset1:40
	v_cvt_pk_bf16_f32 v14, v162, v166
	v_cvt_pk_bf16_f32 v15, v170, v174
	v_add_u32_e32 v160, 0x800, v0
	s_addc_u32 s47, s79, s47
	ds_write2_b32 v160, v14, v15 offset0:64 offset1:72
	v_cvt_pk_bf16_f32 v14, v163, v167
	v_cvt_pk_bf16_f32 v15, v171, v175
	v_add_u32_e32 v0, 0xc00, v0
	s_add_u32 s90, s46, 0x4000
	ds_write2_b32 v0, v14, v15 offset0:96 offset1:104
	s_addc_u32 s91, s47, 0
	v_mov_b32_e32 v0, v192
	global_load_dwordx4 v[160:163], v0, s[46:47] nt
	global_load_dwordx4 v[164:167], v0, s[46:47] offset:1024 nt
	global_load_dwordx4 v[168:171], v0, s[90:91] nt
	global_load_dwordx4 v[172:175], v0, s[90:91] offset:1024 nt
	s_cmp_ge_u32 s49, s40
	s_cselect_b64 s[46:47], -1, 0
	s_and_b32 s25, s2, 0x380
	s_cmp_lt_u32 s49, s40
	s_cselect_b32 s25, s25, 0
	s_add_u32 s90, s25, s54
	s_addc_u32 s91, 0, s55
	s_and_b64 vcc, exec, s[0:1]
	s_cbranch_vccnz .LBB0_1328
	s_waitcnt vmcnt(14)
	v_cvt_pk_f32_fp8_sdwa v[242:243], v210 src0_sel:WORD_1
	v_cvt_pk_f32_fp8_e32 v[244:245], v211
	v_add_u32_e32 v0, s26, v197
	ds_read_b128 v[236:239], v0
	v_cvt_pk_bf16_f32 v241, v242, v243
	v_cvt_pk_bf16_f32 v242, v244, v245
	ds_read_b128 v[244:247], v0 offset:4608
	ds_read_b128 v[198:201], v0 offset:9216
	ds_read_b128 v[202:205], v0 offset:13824
	v_cvt_pk_f32_fp8_e32 v[14:15], v210
	v_cvt_pk_f32_fp8_sdwa v[232:233], v211 src0_sel:WORD_1
	v_cvt_pk_bf16_f32 v240, v14, v15
	v_cvt_pk_bf16_f32 v243, v232, v233
	s_waitcnt vmcnt(12)
	v_cvt_pk_f32_fp8_e32 v[14:15], v248
	v_cvt_pk_f32_fp8_sdwa v[232:233], v248 src0_sel:WORD_1
	s_waitcnt lgkmcnt(3)
	v_mfma_f32_32x32x16_bf16 v[128:143], v[236:239], v[240:243], v[128:143]
	s_waitcnt lgkmcnt(2)
	v_mfma_f32_32x32x16_bf16 v[96:111], v[244:247], v[240:243], v[96:111]
	s_waitcnt lgkmcnt(1)
	v_mfma_f32_32x32x16_bf16 v[112:127], v[198:201], v[240:243], v[112:127]
	s_waitcnt lgkmcnt(0)
	v_mfma_f32_32x32x16_bf16 v[80:95], v[202:205], v[240:243], v[80:95]
	v_cvt_pk_f32_fp8_e32 v[242:243], v249
	v_cvt_pk_f32_fp8_sdwa v[10:11], v249 src0_sel:WORD_1
	v_cvt_pk_bf16_f32 v240, v14, v15
	v_cvt_pk_bf16_f32 v241, v232, v233
	v_cvt_pk_bf16_f32 v242, v242, v243
	v_cvt_pk_bf16_f32 v243, v10, v11
	v_cvt_pk_f32_fp8_e32 v[10:11], v212
	v_cvt_pk_f32_fp8_sdwa v[14:15], v212 src0_sel:WORD_1
	v_mfma_f32_32x32x16_bf16 v[64:79], v[236:239], v[240:243], v[64:79]
	ds_read_b128 v[236:239], v0 offset:16
	v_cvt_pk_bf16_f32 v232, v10, v11
	v_cvt_pk_bf16_f32 v233, v14, v15
	v_cvt_pk_f32_fp8_e32 v[10:11], v250
	v_cvt_pk_f32_fp8_sdwa v[14:15], v250 src0_sel:WORD_1
	v_cvt_pk_bf16_f32 v10, v10, v11
	v_mfma_f32_32x32x16_bf16 v[32:47], v[244:247], v[240:243], v[32:47]
	ds_read_b128 v[244:247], v0 offset:9232
	v_cvt_pk_bf16_f32 v11, v14, v15
	v_cvt_pk_f32_fp8_e32 v[14:15], v207
	v_mfma_f32_32x32x16_bf16 v[48:63], v[198:201], v[240:243], v[48:63]
	ds_read_b128 v[198:201], v0 offset:13840
	v_mfma_f32_32x32x16_bf16 v[16:31], v[202:205], v[240:243], v[16:31]
	v_cvt_pk_f32_fp8_e32 v[240:241], v213
	v_cvt_pk_f32_fp8_sdwa v[242:243], v213 src0_sel:WORD_1
	v_cvt_pk_bf16_f32 v234, v240, v241
	v_cvt_pk_bf16_f32 v235, v242, v243
	ds_read_b128 v[240:243], v0 offset:4624
	s_waitcnt lgkmcnt(3)
	v_mfma_f32_32x32x16_bf16 v[128:143], v[236:239], v[232:235], v[128:143]
	s_waitcnt lgkmcnt(0)
	v_mfma_f32_32x32x16_bf16 v[96:111], v[240:243], v[232:235], v[96:111]
	v_mfma_f32_32x32x16_bf16 v[112:127], v[244:247], v[232:235], v[112:127]
	v_mfma_f32_32x32x16_bf16 v[80:95], v[198:201], v[232:235], v[80:95]
	v_cvt_pk_f32_fp8_e32 v[232:233], v251
	v_cvt_pk_f32_fp8_sdwa v[234:235], v251 src0_sel:WORD_1
	v_cvt_pk_bf16_f32 v12, v232, v233
	v_cvt_pk_bf16_f32 v13, v234, v235
	ds_read_b128 v[232:235], v0 offset:32
	s_nop 0
	v_mfma_f32_32x32x16_bf16 v[64:79], v[236:239], v[10:13], v[64:79]
	ds_read_b128 v[236:239], v0 offset:4640
	v_mfma_f32_32x32x16_bf16 v[32:47], v[240:243], v[10:13], v[32:47]
	ds_read_b128 v[240:243], v0 offset:9248
	v_mfma_f32_32x32x16_bf16 v[48:63], v[244:247], v[10:13], v[48:63]
	ds_read_b128 v[244:247], v0 offset:13856
	v_mfma_f32_32x32x16_bf16 v[16:31], v[198:201], v[10:13], v[16:31]
	v_cvt_pk_f32_fp8_e32 v[10:11], v206
	v_cvt_pk_f32_fp8_sdwa v[12:13], v206 src0_sel:WORD_1
	v_cvt_pk_f32_fp8_sdwa v[6:7], v207 src0_sel:WORD_1
	v_cvt_pk_bf16_f32 v10, v10, v11
	v_cvt_pk_bf16_f32 v11, v12, v13
	v_cvt_pk_bf16_f32 v12, v14, v15
	v_cvt_pk_bf16_f32 v13, v6, v7
	v_cvt_pk_f32_fp8_e32 v[6:7], v214
	v_cvt_pk_f32_fp8_e32 v[14:15], v215
	s_waitcnt lgkmcnt(3)
	v_mfma_f32_32x32x16_bf16 v[128:143], v[232:235], v[10:13], v[128:143]
	s_waitcnt lgkmcnt(2)
	v_mfma_f32_32x32x16_bf16 v[96:111], v[236:239], v[10:13], v[96:111]
	s_waitcnt lgkmcnt(1)
	v_mfma_f32_32x32x16_bf16 v[112:127], v[240:243], v[10:13], v[112:127]
	s_waitcnt lgkmcnt(0)
	v_mfma_f32_32x32x16_bf16 v[80:95], v[244:247], v[10:13], v[80:95]
	v_cvt_pk_f32_fp8_sdwa v[12:13], v214 src0_sel:WORD_1
	v_cvt_pk_f32_fp8_sdwa v[2:3], v215 src0_sel:WORD_1
	v_cvt_pk_bf16_f32 v10, v6, v7
	v_cvt_pk_bf16_f32 v11, v12, v13
	v_cvt_pk_bf16_f32 v12, v14, v15
	v_cvt_pk_bf16_f32 v13, v2, v3
	v_cvt_pk_f32_fp8_e32 v[2:3], v208
	v_cvt_pk_f32_fp8_sdwa v[14:15], v209 src0_sel:WORD_1
	v_mfma_f32_32x32x16_bf16 v[64:79], v[232:235], v[10:13], v[64:79]
	ds_read_b128 v[232:235], v0 offset:48
	v_cvt_pk_bf16_f32 v6, v2, v3
	v_cvt_pk_f32_fp8_e32 v[2:3], v216
	v_cvt_pk_bf16_f32 v2, v2, v3
	v_mfma_f32_32x32x16_bf16 v[32:47], v[236:239], v[10:13], v[32:47]
	ds_read_b128 v[236:239], v0 offset:9264
	v_mfma_f32_32x32x16_bf16 v[48:63], v[240:243], v[10:13], v[48:63]
	ds_read_b128 v[240:243], v0 offset:13872
	v_mfma_f32_32x32x16_bf16 v[16:31], v[244:247], v[10:13], v[16:31]
	v_cvt_pk_f32_fp8_sdwa v[10:11], v208 src0_sel:WORD_1
	v_cvt_pk_f32_fp8_e32 v[12:13], v209
	v_cvt_pk_bf16_f32 v9, v14, v15
	v_cvt_pk_f32_fp8_sdwa v[14:15], v217 src0_sel:WORD_1
	v_cvt_pk_bf16_f32 v7, v10, v11
	v_cvt_pk_bf16_f32 v8, v12, v13
	ds_read_b128 v[10:13], v0 offset:4656
	s_waitcnt lgkmcnt(3)
	v_mfma_f32_32x32x16_bf16 v[128:143], v[232:235], v[6:9], v[128:143]
	s_waitcnt lgkmcnt(0)
	v_mfma_f32_32x32x16_bf16 v[96:111], v[10:13], v[6:9], v[96:111]
	v_mfma_f32_32x32x16_bf16 v[112:127], v[236:239], v[6:9], v[112:127]
	v_mfma_f32_32x32x16_bf16 v[80:95], v[240:243], v[6:9], v[80:95]
	v_cvt_pk_f32_fp8_sdwa v[6:7], v216 src0_sel:WORD_1
	v_cvt_pk_f32_fp8_e32 v[8:9], v217
	v_cvt_pk_bf16_f32 v5, v14, v15
	v_cvt_pk_bf16_f32 v3, v6, v7
	v_cvt_pk_bf16_f32 v4, v8, v9
	s_nop 1
	v_mfma_f32_32x32x16_bf16 v[64:79], v[232:235], v[2:5], v[64:79]
	v_mfma_f32_32x32x16_bf16 v[32:47], v[10:13], v[2:5], v[32:47]
	v_mfma_f32_32x32x16_bf16 v[48:63], v[236:239], v[2:5], v[48:63]
	v_mfma_f32_32x32x16_bf16 v[16:31], v[240:243], v[2:5], v[16:31]
.LBB0_1328:
	s_add_i32 s25, s49, -2
	s_and_b32 s26, s25, 14
	s_cmp_lg_u32 s26, 14
	s_cbranch_scc1 .LBB0_1323
	s_and_b64 vcc, exec, s[0:1]
	v_mbcnt_lo_u32_b32 v0, -1, 0
	v_mbcnt_hi_u32_b32 v0, -1, v0
	s_cbranch_vccnz .LBB0_1323
	v_and_b32_e32 v2, 31, v0
	v_lshl_add_u32 v6, v2, 2, s86
	v_ashrrev_i32_e32 v0, 1, v0
	v_and_b32_e32 v2, -16, v0
	ds_read_b32 v0, v6 offset:55296
	s_lshr_b32 s0, s25, 4
	s_add_i32 s0, s0, s76
	s_and_b32 s0, s0, s77
	s_add_i32 s0, s0, s27
	s_waitcnt lgkmcnt(0)
	v_lshlrev_b64 v[4:5], 8, v[0:1]
	v_mul_f32_e32 v0, 0xbfb8aa3b, v128
	v_exp_f32_e32 v0, v0
	s_lshl_b32 s0, s0, 6
	s_add_u32 s0, s58, s0
	s_addc_u32 s1, s59, 0
	v_ashrrev_i32_e32 v3, 31, v2
	v_add_f32_e32 v0, 1.0, v0
	v_lshl_add_u64 v[2:3], s[0:1], 0, v[2:3]
	v_div_scale_f32 v7, s[0:1], v0, v0, v128
	v_rcp_f32_e32 v8, v7
	v_lshl_add_u64 v[4:5], v[2:3], 0, v[4:5]
	v_fma_f32 v9, -v7, v8, 1.0
	v_fmac_f32_e32 v8, v9, v8
	v_div_scale_f32 v9, vcc, v128, v0, v128
	s_waitcnt vmcnt(8)
	v_mul_f32_e32 v10, v9, v8
	v_fma_f32 v11, -v7, v10, v9
	v_fmac_f32_e32 v10, v11, v8
	v_fma_f32 v7, -v7, v10, v9
	v_div_fmas_f32 v7, v7, v8, v10
	v_div_fixup_f32 v0, v7, v0, v128
	v_mul_f32_e32 v7, 0xbfb8aa3b, v132
	v_exp_f32_e32 v7, v7
	v_mul_f32_e32 v0, v112, v0
	v_add_f32_e32 v7, 1.0, v7
	v_div_scale_f32 v8, s[0:1], v7, v7, v132
	v_rcp_f32_e32 v9, v8
	s_nop 0
	v_fma_f32 v10, -v8, v9, 1.0
	v_fmac_f32_e32 v9, v10, v9
	v_div_scale_f32 v10, vcc, v132, v7, v132
	v_mul_f32_e32 v11, v10, v9
	v_fma_f32 v12, -v8, v11, v10
	v_fmac_f32_e32 v11, v12, v9
	v_fma_f32 v8, -v8, v11, v10
	v_div_fmas_f32 v8, v8, v9, v11
	v_div_fixup_f32 v7, v8, v7, v132
	v_mul_f32_e32 v8, 0xbfb8aa3b, v136
	v_exp_f32_e32 v8, v8
	v_mul_f32_e32 v7, v116, v7
	v_add_f32_e32 v8, 1.0, v8
	v_div_scale_f32 v9, s[0:1], v8, v8, v136
	v_rcp_f32_e32 v10, v9
	s_nop 0
	v_fma_f32 v11, -v9, v10, 1.0
	v_fmac_f32_e32 v10, v11, v10
	v_div_scale_f32 v11, vcc, v136, v8, v136
	v_mul_f32_e32 v12, v11, v10
	v_fma_f32 v13, -v9, v12, v11
	v_fmac_f32_e32 v12, v13, v10
	v_fma_f32 v9, -v9, v12, v11
	v_div_fmas_f32 v9, v9, v10, v12
	v_div_fixup_f32 v8, v9, v8, v136
	v_mul_f32_e32 v9, 0xbfb8aa3b, v140
	v_exp_f32_e32 v9, v9
	v_mul_f32_e32 v8, v120, v8
	v_add_f32_e32 v9, 1.0, v9
	v_div_scale_f32 v10, s[0:1], v9, v9, v140
	v_rcp_f32_e32 v11, v10
	s_nop 0
	v_fma_f32 v12, -v10, v11, 1.0
	v_fmac_f32_e32 v11, v12, v11
	v_div_scale_f32 v12, vcc, v140, v9, v140
	v_mul_f32_e32 v13, v12, v11
	v_fma_f32 v14, -v10, v13, v12
	v_fmac_f32_e32 v13, v14, v11
	v_fma_f32 v10, -v10, v13, v12
	v_div_fmas_f32 v10, v10, v11, v13
	v_div_fixup_f32 v9, v10, v9, v140
	v_mul_f32_e32 v10, 0xbfb8aa3b, v129
	v_exp_f32_e32 v10, v10
	v_mul_f32_e32 v9, v124, v9
	v_add_f32_e32 v10, 1.0, v10
	v_div_scale_f32 v11, s[0:1], v10, v10, v129
	v_rcp_f32_e32 v12, v11
	s_nop 0
	v_fma_f32 v13, -v11, v12, 1.0
	v_fmac_f32_e32 v12, v13, v12
	v_div_scale_f32 v13, vcc, v129, v10, v129
	v_mul_f32_e32 v14, v13, v12
	v_fma_f32 v15, -v11, v14, v13
	v_fmac_f32_e32 v14, v15, v12
	v_fma_f32 v11, -v11, v14, v13
	v_div_fmas_f32 v11, v11, v12, v14
	v_div_fixup_f32 v10, v11, v10, v129
	v_mul_f32_e32 v11, 0xbfb8aa3b, v133
	v_exp_f32_e32 v11, v11
	v_mul_f32_e32 v10, v113, v10
	v_add_f32_e32 v11, 1.0, v11
	v_div_scale_f32 v12, s[0:1], v11, v11, v133
	v_rcp_f32_e32 v13, v12
	s_nop 0
	v_fma_f32 v14, -v12, v13, 1.0
	v_fmac_f32_e32 v13, v14, v13
	v_div_scale_f32 v14, vcc, v133, v11, v133
	v_mul_f32_e32 v15, v14, v13
	v_fma_f32 v112, -v12, v15, v14
	v_fmac_f32_e32 v15, v112, v13
	v_fma_f32 v12, -v12, v15, v14
	v_div_fmas_f32 v12, v12, v13, v15
	v_div_fixup_f32 v11, v12, v11, v133
	v_mul_f32_e32 v12, 0xbfb8aa3b, v137
	v_exp_f32_e32 v12, v12
	v_mul_f32_e32 v11, v117, v11
	v_add_f32_e32 v12, 1.0, v12
	v_div_scale_f32 v13, s[0:1], v12, v12, v137
	v_rcp_f32_e32 v14, v13
	s_nop 0
	v_fma_f32 v15, -v13, v14, 1.0
	v_fmac_f32_e32 v14, v15, v14
	v_div_scale_f32 v15, vcc, v137, v12, v137
	v_mul_f32_e32 v112, v15, v14
	v_fma_f32 v113, -v13, v112, v15
	v_fmac_f32_e32 v112, v113, v14
	v_fma_f32 v13, -v13, v112, v15
	v_div_fmas_f32 v13, v13, v14, v112
	v_div_fixup_f32 v12, v13, v12, v137
	v_mul_f32_e32 v13, 0xbfb8aa3b, v141
	v_exp_f32_e32 v13, v13
	v_mul_f32_e32 v12, v121, v12
	v_add_f32_e32 v13, 1.0, v13
	v_div_scale_f32 v14, s[0:1], v13, v13, v141
	v_rcp_f32_e32 v15, v14
	s_nop 0
	v_fma_f32 v112, -v14, v15, 1.0
	v_fmac_f32_e32 v15, v112, v15
	v_div_scale_f32 v112, vcc, v141, v13, v141
	v_mul_f32_e32 v113, v112, v15
	v_fma_f32 v116, -v14, v113, v112
	v_fmac_f32_e32 v113, v116, v15
	v_fma_f32 v14, -v14, v113, v112
	v_div_fmas_f32 v14, v14, v15, v113
	v_div_fixup_f32 v13, v14, v13, v141
	v_mul_f32_e32 v14, 0xbfb8aa3b, v130
	v_exp_f32_e32 v14, v14
	v_mul_f32_e32 v13, v125, v13
	v_add_f32_e32 v14, 1.0, v14
	v_div_scale_f32 v15, s[0:1], v14, v14, v130
	v_rcp_f32_e32 v112, v15
	s_nop 0
	v_fma_f32 v113, -v15, v112, 1.0
	v_fmac_f32_e32 v112, v113, v112
	v_div_scale_f32 v113, vcc, v130, v14, v130
	v_mul_f32_e32 v116, v113, v112
	v_fma_f32 v117, -v15, v116, v113
	v_fmac_f32_e32 v116, v117, v112
	v_fma_f32 v15, -v15, v116, v113
	v_div_fmas_f32 v15, v15, v112, v116
	v_div_fixup_f32 v14, v15, v14, v130
	v_mul_f32_e32 v15, 0xbfb8aa3b, v134
	v_exp_f32_e32 v15, v15
	v_mul_f32_e32 v14, v114, v14
	v_add_f32_e32 v15, 1.0, v15
	v_div_scale_f32 v112, s[0:1], v15, v15, v134
	v_rcp_f32_e32 v113, v112
	s_nop 0
	v_fma_f32 v114, -v112, v113, 1.0
	v_fmac_f32_e32 v113, v114, v113
	v_div_scale_f32 v114, vcc, v134, v15, v134
	v_mul_f32_e32 v116, v114, v113
	v_fma_f32 v117, -v112, v116, v114
	v_fmac_f32_e32 v116, v117, v113
	v_fma_f32 v112, -v112, v116, v114
	v_div_fmas_f32 v112, v112, v113, v116
	v_div_fixup_f32 v15, v112, v15, v134
	v_mul_f32_e32 v112, 0xbfb8aa3b, v138
	v_exp_f32_e32 v112, v112
	v_mul_f32_e32 v15, v118, v15
	v_add_f32_e32 v112, 1.0, v112
	v_div_scale_f32 v113, s[0:1], v112, v112, v138
	v_rcp_f32_e32 v114, v113
	s_nop 0
	v_fma_f32 v116, -v113, v114, 1.0
	v_fmac_f32_e32 v114, v116, v114
	v_div_scale_f32 v116, vcc, v138, v112, v138
	v_mul_f32_e32 v117, v116, v114
	v_fma_f32 v118, -v113, v117, v116
	v_fmac_f32_e32 v117, v118, v114
	v_fma_f32 v113, -v113, v117, v116
	v_div_fmas_f32 v113, v113, v114, v117
	v_div_fixup_f32 v112, v113, v112, v138
	v_mul_f32_e32 v116, v122, v112
	v_mul_f32_e32 v112, 0xbfb8aa3b, v142
	v_exp_f32_e32 v112, v112
	s_nop 0
	v_add_f32_e32 v112, 1.0, v112
	v_div_scale_f32 v113, s[0:1], v112, v112, v142
	v_rcp_f32_e32 v114, v113
	s_nop 0
	v_fma_f32 v117, -v113, v114, 1.0
	v_fmac_f32_e32 v114, v117, v114
	v_div_scale_f32 v117, vcc, v142, v112, v142
	v_mul_f32_e32 v118, v117, v114
	v_fma_f32 v120, -v113, v118, v117
	v_fmac_f32_e32 v118, v120, v114
	v_fma_f32 v113, -v113, v118, v117
	v_div_fmas_f32 v113, v113, v114, v118
	v_div_fixup_f32 v112, v113, v112, v142
	v_mul_f32_e32 v117, v126, v112
	v_mul_f32_e32 v112, 0xbfb8aa3b, v131
	v_exp_f32_e32 v112, v112
	s_nop 0
	v_add_f32_e32 v112, 1.0, v112
	v_div_scale_f32 v113, s[0:1], v112, v112, v131
	v_rcp_f32_e32 v114, v113
	s_nop 0
	v_fma_f32 v118, -v113, v114, 1.0
	v_fmac_f32_e32 v114, v118, v114
	v_div_scale_f32 v118, vcc, v131, v112, v131
	v_mul_f32_e32 v120, v118, v114
	v_fma_f32 v121, -v113, v120, v118
	v_fmac_f32_e32 v120, v121, v114
	v_fma_f32 v113, -v113, v120, v118
	v_div_fmas_f32 v113, v113, v114, v120
	v_div_fixup_f32 v112, v113, v112, v131
	v_mul_f32_e32 v118, v115, v112
	v_mul_f32_e32 v112, 0xbfb8aa3b, v135
	v_exp_f32_e32 v112, v112
	s_nop 0
	v_add_f32_e32 v112, 1.0, v112
	v_div_scale_f32 v113, s[0:1], v112, v112, v135
	v_rcp_f32_e32 v114, v113
	s_nop 0
	v_fma_f32 v115, -v113, v114, 1.0
	v_fmac_f32_e32 v114, v115, v114
	v_div_scale_f32 v115, vcc, v135, v112, v135
	v_mul_f32_e32 v120, v115, v114
	v_fma_f32 v121, -v113, v120, v115
	v_fmac_f32_e32 v120, v121, v114
	v_fma_f32 v113, -v113, v120, v115
	v_div_fmas_f32 v113, v113, v114, v120
	v_div_fixup_f32 v112, v113, v112, v135
	v_mul_f32_e32 v119, v119, v112
	v_mul_f32_e32 v112, 0xbfb8aa3b, v139
	v_exp_f32_e32 v112, v112
	s_nop 0
	v_add_f32_e32 v112, 1.0, v112
	v_div_scale_f32 v113, s[0:1], v112, v112, v139
	v_rcp_f32_e32 v114, v113
	s_nop 0
	v_fma_f32 v115, -v113, v114, 1.0
	v_fmac_f32_e32 v114, v115, v114
	v_div_scale_f32 v115, vcc, v139, v112, v139
	v_mul_f32_e32 v120, v115, v114
	v_fma_f32 v121, -v113, v120, v115
	v_fmac_f32_e32 v120, v121, v114
	v_fma_f32 v113, -v113, v120, v115
	v_div_fmas_f32 v113, v113, v114, v120
	v_div_fixup_f32 v112, v113, v112, v139
	v_mul_f32_e32 v120, v123, v112
	v_mul_f32_e32 v112, 0xbfb8aa3b, v143
	v_exp_f32_e32 v112, v112
	s_nop 0
	v_add_f32_e32 v112, 1.0, v112
	v_div_scale_f32 v113, s[0:1], v112, v112, v143
	v_rcp_f32_e32 v114, v113
	s_nop 0
	v_fma_f32 v115, -v113, v114, 1.0
	v_fmac_f32_e32 v114, v115, v114
	v_div_scale_f32 v115, vcc, v143, v112, v143
	v_mul_f32_e32 v121, v115, v114
	v_fma_f32 v122, -v113, v121, v115
	v_fmac_f32_e32 v121, v122, v114
	v_fma_f32 v113, -v113, v121, v115
	v_div_fmas_f32 v113, v113, v114, v121
	v_div_fixup_f32 v112, v113, v112, v143
	v_mul_f32_e32 v121, v127, v112
	v_mov_b32_e32 v112, v1
	v_cvt_pk_fp8_f32 v112, v0, v7
	v_mul_f32_e32 v0, 0xbfb8aa3b, v96
	v_exp_f32_e32 v0, v0
	v_mov_b32_e32 v113, v1
	v_cvt_pk_fp8_f32 v112, v8, v9 op_sel:[0,0,1]
	v_cvt_pk_fp8_f32 v113, v10, v11
	v_add_f32_e32 v0, 1.0, v0
	v_div_scale_f32 v7, s[0:1], v0, v0, v96
	v_rcp_f32_e32 v8, v7
	v_cvt_pk_fp8_f32 v113, v12, v13 op_sel:[0,0,1]
	v_mov_b32_e32 v114, v1
	v_cvt_pk_fp8_f32 v114, v14, v15
	v_fma_f32 v9, -v7, v8, 1.0
	v_fmac_f32_e32 v8, v9, v8
	v_div_scale_f32 v9, vcc, v96, v0, v96
	v_mul_f32_e32 v10, v9, v8
	v_fma_f32 v11, -v7, v10, v9
	v_fmac_f32_e32 v10, v11, v8
	v_fma_f32 v7, -v7, v10, v9
	v_div_fmas_f32 v7, v7, v8, v10
	v_div_fixup_f32 v0, v7, v0, v96
	v_mul_f32_e32 v7, 0xbfb8aa3b, v100
	v_exp_f32_e32 v7, v7
	v_mul_f32_e32 v0, v80, v0
	v_mov_b32_e32 v115, v1
	v_cvt_pk_fp8_f32 v115, v118, v119
	v_add_f32_e32 v7, 1.0, v7
	v_div_scale_f32 v8, s[0:1], v7, v7, v100
	v_rcp_f32_e32 v9, v8
	v_cvt_pk_fp8_f32 v114, v116, v117 op_sel:[0,0,1]
	v_cvt_pk_fp8_f32 v115, v120, v121 op_sel:[0,0,1]
	v_fma_f32 v10, -v8, v9, 1.0
	v_fmac_f32_e32 v9, v10, v9
	v_div_scale_f32 v10, vcc, v100, v7, v100
	v_mul_f32_e32 v11, v10, v9
	v_fma_f32 v12, -v8, v11, v10
	v_fmac_f32_e32 v11, v12, v9
	v_fma_f32 v8, -v8, v11, v10
	v_div_fmas_f32 v8, v8, v9, v11
	v_div_fixup_f32 v7, v8, v7, v100
	v_mul_f32_e32 v8, 0xbfb8aa3b, v104
	v_exp_f32_e32 v8, v8
	v_mul_f32_e32 v7, v84, v7
	global_store_dwordx4 v[4:5], v[112:115], off
	v_add_f32_e32 v8, 1.0, v8
	v_div_scale_f32 v9, s[0:1], v8, v8, v104
	v_rcp_f32_e32 v10, v9
	s_nop 0
	v_fma_f32 v11, -v9, v10, 1.0
	v_fmac_f32_e32 v10, v11, v10
	v_div_scale_f32 v11, vcc, v104, v8, v104
	v_mul_f32_e32 v12, v11, v10
	v_fma_f32 v13, -v9, v12, v11
	v_fmac_f32_e32 v12, v13, v10
	v_fma_f32 v9, -v9, v12, v11
	v_div_fmas_f32 v9, v9, v10, v12
	v_div_fixup_f32 v8, v9, v8, v104
	v_mul_f32_e32 v9, 0xbfb8aa3b, v108
	v_exp_f32_e32 v9, v9
	v_mul_f32_e32 v8, v88, v8
	v_add_f32_e32 v9, 1.0, v9
	v_div_scale_f32 v10, s[0:1], v9, v9, v108
	v_rcp_f32_e32 v11, v10
	s_nop 0
	v_fma_f32 v12, -v10, v11, 1.0
	v_fmac_f32_e32 v11, v12, v11
	v_div_scale_f32 v12, vcc, v108, v9, v108
	v_mul_f32_e32 v13, v12, v11
	v_fma_f32 v14, -v10, v13, v12
	v_fmac_f32_e32 v13, v14, v11
	v_fma_f32 v10, -v10, v13, v12
	v_div_fmas_f32 v10, v10, v11, v13
	v_div_fixup_f32 v9, v10, v9, v108
	v_mul_f32_e32 v10, 0xbfb8aa3b, v97
	v_exp_f32_e32 v10, v10
	v_mul_f32_e32 v9, v92, v9
	v_add_f32_e32 v10, 1.0, v10
	v_div_scale_f32 v11, s[0:1], v10, v10, v97
	v_rcp_f32_e32 v12, v11
	s_nop 0
	v_fma_f32 v13, -v11, v12, 1.0
	v_fmac_f32_e32 v12, v13, v12
	v_div_scale_f32 v13, vcc, v97, v10, v97
	v_mul_f32_e32 v14, v13, v12
	v_fma_f32 v15, -v11, v14, v13
	v_fmac_f32_e32 v14, v15, v12
	v_fma_f32 v11, -v11, v14, v13
	v_div_fmas_f32 v11, v11, v12, v14
	v_div_fixup_f32 v10, v11, v10, v97
	v_mul_f32_e32 v11, 0xbfb8aa3b, v101
	v_exp_f32_e32 v11, v11
	v_mul_f32_e32 v10, v81, v10
	v_add_f32_e32 v11, 1.0, v11
	v_div_scale_f32 v12, s[0:1], v11, v11, v101
	v_rcp_f32_e32 v13, v12
	s_nop 0
	v_fma_f32 v14, -v12, v13, 1.0
	v_fmac_f32_e32 v13, v14, v13
	v_div_scale_f32 v14, vcc, v101, v11, v101
	v_mul_f32_e32 v15, v14, v13
	v_fma_f32 v80, -v12, v15, v14
	v_fmac_f32_e32 v15, v80, v13
	v_fma_f32 v12, -v12, v15, v14
	v_div_fmas_f32 v12, v12, v13, v15
	v_div_fixup_f32 v11, v12, v11, v101
	v_mul_f32_e32 v12, 0xbfb8aa3b, v105
	v_exp_f32_e32 v12, v12
	v_mul_f32_e32 v11, v85, v11
	v_add_f32_e32 v12, 1.0, v12
	v_div_scale_f32 v13, s[0:1], v12, v12, v105
	v_rcp_f32_e32 v14, v13
	s_nop 0
	v_fma_f32 v15, -v13, v14, 1.0
	v_fmac_f32_e32 v14, v15, v14
	v_div_scale_f32 v15, vcc, v105, v12, v105
	v_mul_f32_e32 v80, v15, v14
	v_fma_f32 v81, -v13, v80, v15
	v_fmac_f32_e32 v80, v81, v14
	v_fma_f32 v13, -v13, v80, v15
	v_div_fmas_f32 v13, v13, v14, v80
	v_div_fixup_f32 v12, v13, v12, v105
	v_mul_f32_e32 v13, 0xbfb8aa3b, v109
	v_exp_f32_e32 v13, v13
	v_mul_f32_e32 v12, v89, v12
	v_add_f32_e32 v13, 1.0, v13
	v_div_scale_f32 v14, s[0:1], v13, v13, v109
	v_rcp_f32_e32 v15, v14
	s_nop 0
	v_fma_f32 v80, -v14, v15, 1.0
	v_fmac_f32_e32 v15, v80, v15
	v_div_scale_f32 v80, vcc, v109, v13, v109
	v_mul_f32_e32 v81, v80, v15
	v_fma_f32 v84, -v14, v81, v80
	v_fmac_f32_e32 v81, v84, v15
	v_fma_f32 v14, -v14, v81, v80
	v_div_fmas_f32 v14, v14, v15, v81
	v_div_fixup_f32 v13, v14, v13, v109
	v_mul_f32_e32 v14, 0xbfb8aa3b, v98
	v_exp_f32_e32 v14, v14
	v_mul_f32_e32 v13, v93, v13
	v_add_f32_e32 v14, 1.0, v14
	v_div_scale_f32 v15, s[0:1], v14, v14, v98
	v_rcp_f32_e32 v80, v15
	s_nop 0
	v_fma_f32 v81, -v15, v80, 1.0
	v_fmac_f32_e32 v80, v81, v80
	v_div_scale_f32 v81, vcc, v98, v14, v98
	v_mul_f32_e32 v84, v81, v80
	v_fma_f32 v85, -v15, v84, v81
	v_fmac_f32_e32 v84, v85, v80
	v_fma_f32 v15, -v15, v84, v81
	v_div_fmas_f32 v15, v15, v80, v84
	v_div_fixup_f32 v14, v15, v14, v98
	v_mul_f32_e32 v15, 0xbfb8aa3b, v102
	v_exp_f32_e32 v15, v15
	v_mul_f32_e32 v14, v82, v14
	v_add_f32_e32 v15, 1.0, v15
	v_div_scale_f32 v80, s[0:1], v15, v15, v102
	v_rcp_f32_e32 v81, v80
	s_nop 0
	v_fma_f32 v82, -v80, v81, 1.0
	v_fmac_f32_e32 v81, v82, v81
	v_div_scale_f32 v82, vcc, v102, v15, v102
	v_mul_f32_e32 v84, v82, v81
	v_fma_f32 v85, -v80, v84, v82
	v_fmac_f32_e32 v84, v85, v81
	v_fma_f32 v80, -v80, v84, v82
	v_div_fmas_f32 v80, v80, v81, v84
	v_div_fixup_f32 v15, v80, v15, v102
	v_mul_f32_e32 v80, 0xbfb8aa3b, v106
	v_exp_f32_e32 v80, v80
	v_mul_f32_e32 v15, v86, v15
	v_add_f32_e32 v80, 1.0, v80
	v_div_scale_f32 v81, s[0:1], v80, v80, v106
	v_rcp_f32_e32 v82, v81
	s_nop 0
	v_fma_f32 v84, -v81, v82, 1.0
	v_fmac_f32_e32 v82, v84, v82
	v_div_scale_f32 v84, vcc, v106, v80, v106
	v_mul_f32_e32 v85, v84, v82
	v_fma_f32 v86, -v81, v85, v84
	v_fmac_f32_e32 v85, v86, v82
	v_fma_f32 v81, -v81, v85, v84
	v_div_fmas_f32 v81, v81, v82, v85
	v_div_fixup_f32 v80, v81, v80, v106
	v_mul_f32_e32 v84, v90, v80
	v_mul_f32_e32 v80, 0xbfb8aa3b, v110
	v_exp_f32_e32 v80, v80
	s_nop 0
	v_add_f32_e32 v80, 1.0, v80
	v_div_scale_f32 v81, s[0:1], v80, v80, v110
	v_rcp_f32_e32 v82, v81
	s_nop 0
	v_fma_f32 v85, -v81, v82, 1.0
	v_fmac_f32_e32 v82, v85, v82
	v_div_scale_f32 v85, vcc, v110, v80, v110
	v_mul_f32_e32 v86, v85, v82
	v_fma_f32 v88, -v81, v86, v85
	v_fmac_f32_e32 v86, v88, v82
	v_fma_f32 v81, -v81, v86, v85
	v_div_fmas_f32 v81, v81, v82, v86
	v_div_fixup_f32 v80, v81, v80, v110
	v_mul_f32_e32 v85, v94, v80
	v_mul_f32_e32 v80, 0xbfb8aa3b, v99
	v_exp_f32_e32 v80, v80
	s_nop 0
	v_add_f32_e32 v80, 1.0, v80
	v_div_scale_f32 v81, s[0:1], v80, v80, v99
	v_rcp_f32_e32 v82, v81
	s_nop 0
	v_fma_f32 v86, -v81, v82, 1.0
	v_fmac_f32_e32 v82, v86, v82
	v_div_scale_f32 v86, vcc, v99, v80, v99
	v_mul_f32_e32 v88, v86, v82
	v_fma_f32 v89, -v81, v88, v86
	v_fmac_f32_e32 v88, v89, v82
	v_fma_f32 v81, -v81, v88, v86
	v_div_fmas_f32 v81, v81, v82, v88
	v_div_fixup_f32 v80, v81, v80, v99
	v_mul_f32_e32 v86, v83, v80
	v_mul_f32_e32 v80, 0xbfb8aa3b, v103
	v_exp_f32_e32 v80, v80
	s_nop 0
	v_add_f32_e32 v80, 1.0, v80
	v_div_scale_f32 v81, s[0:1], v80, v80, v103
	v_rcp_f32_e32 v82, v81
	s_nop 0
	v_fma_f32 v83, -v81, v82, 1.0
	v_fmac_f32_e32 v82, v83, v82
	v_div_scale_f32 v83, vcc, v103, v80, v103
	v_mul_f32_e32 v88, v83, v82
	v_fma_f32 v89, -v81, v88, v83
	v_fmac_f32_e32 v88, v89, v82
	v_fma_f32 v81, -v81, v88, v83
	v_div_fmas_f32 v81, v81, v82, v88
	v_div_fixup_f32 v80, v81, v80, v103
	v_mul_f32_e32 v87, v87, v80
	v_mul_f32_e32 v80, 0xbfb8aa3b, v107
	v_exp_f32_e32 v80, v80
	s_nop 0
	v_add_f32_e32 v80, 1.0, v80
	v_div_scale_f32 v81, s[0:1], v80, v80, v107
	v_rcp_f32_e32 v82, v81
	s_nop 0
	v_fma_f32 v83, -v81, v82, 1.0
	v_fmac_f32_e32 v82, v83, v82
	v_div_scale_f32 v83, vcc, v107, v80, v107
	v_mul_f32_e32 v88, v83, v82
	v_fma_f32 v89, -v81, v88, v83
	v_fmac_f32_e32 v88, v89, v82
	v_fma_f32 v81, -v81, v88, v83
	v_div_fmas_f32 v81, v81, v82, v88
	v_div_fixup_f32 v80, v81, v80, v107
	v_mul_f32_e32 v88, v91, v80
	v_mul_f32_e32 v80, 0xbfb8aa3b, v111
	v_exp_f32_e32 v80, v80
	s_nop 0
	v_add_f32_e32 v80, 1.0, v80
	v_div_scale_f32 v81, s[0:1], v80, v80, v111
	v_rcp_f32_e32 v82, v81
	s_nop 0
	v_fma_f32 v83, -v81, v82, 1.0
	v_fmac_f32_e32 v82, v83, v82
	v_div_scale_f32 v83, vcc, v111, v80, v111
	v_mul_f32_e32 v89, v83, v82
	v_fma_f32 v90, -v81, v89, v83
	v_fmac_f32_e32 v89, v90, v82
	v_fma_f32 v81, -v81, v89, v83
	v_div_fmas_f32 v81, v81, v82, v89
	v_div_fixup_f32 v80, v81, v80, v111
	v_mul_f32_e32 v89, v95, v80
	v_mov_b32_e32 v80, v1
	v_mov_b32_e32 v81, v1
	v_mov_b32_e32 v82, v1
	v_mov_b32_e32 v83, v1
	v_cvt_pk_fp8_f32 v80, v0, v7
	v_cvt_pk_fp8_f32 v81, v10, v11
	v_cvt_pk_fp8_f32 v82, v14, v15
	v_cvt_pk_fp8_f32 v83, v86, v87
	v_cvt_pk_fp8_f32 v80, v8, v9 op_sel:[0,0,1]
	v_cvt_pk_fp8_f32 v81, v12, v13 op_sel:[0,0,1]
	v_cvt_pk_fp8_f32 v82, v84, v85 op_sel:[0,0,1]
	v_cvt_pk_fp8_f32 v83, v88, v89 op_sel:[0,0,1]
	s_andn2_b64 vcc, exec, s[44:45]
	global_store_dwordx4 v[4:5], v[80:83], off offset:32
	s_cbranch_vccnz .LBB0_1322
	ds_read_b32 v0, v6 offset:55424
	s_waitcnt lgkmcnt(0)
	v_lshlrev_b64 v[4:5], 8, v[0:1]
	v_mul_f32_e32 v0, 0xbfb8aa3b, v64
	v_exp_f32_e32 v0, v0
	v_lshl_add_u64 v[2:3], v[2:3], 0, v[4:5]
	v_add_f32_e32 v0, 1.0, v0
	v_div_scale_f32 v4, s[0:1], v0, v0, v64
	v_rcp_f32_e32 v5, v4
	s_nop 0
	v_fma_f32 v6, -v4, v5, 1.0
	v_fmac_f32_e32 v5, v6, v5
	v_div_scale_f32 v6, vcc, v64, v0, v64
	v_mul_f32_e32 v7, v6, v5
	v_fma_f32 v8, -v4, v7, v6
	v_fmac_f32_e32 v7, v8, v5
	v_fma_f32 v4, -v4, v7, v6
	v_div_fmas_f32 v4, v4, v5, v7
	v_div_fixup_f32 v0, v4, v0, v64
	v_mul_f32_e32 v4, 0xbfb8aa3b, v68
	v_exp_f32_e32 v4, v4
	v_mul_f32_e32 v0, v48, v0
	v_add_f32_e32 v4, 1.0, v4
	v_div_scale_f32 v5, s[0:1], v4, v4, v68
	v_rcp_f32_e32 v6, v5
	s_nop 0
	v_fma_f32 v7, -v5, v6, 1.0
	v_fmac_f32_e32 v6, v7, v6
	v_div_scale_f32 v7, vcc, v68, v4, v68
	v_mul_f32_e32 v8, v7, v6
	v_fma_f32 v9, -v5, v8, v7
	v_fmac_f32_e32 v8, v9, v6
	v_fma_f32 v5, -v5, v8, v7
	v_div_fmas_f32 v5, v5, v6, v8
	v_div_fixup_f32 v4, v5, v4, v68
	v_mul_f32_e32 v5, 0xbfb8aa3b, v72
	v_exp_f32_e32 v5, v5
	v_mul_f32_e32 v4, v52, v4
	v_add_f32_e32 v5, 1.0, v5
	v_div_scale_f32 v6, s[0:1], v5, v5, v72
	v_rcp_f32_e32 v7, v6
	s_nop 0
	v_fma_f32 v8, -v6, v7, 1.0
	v_fmac_f32_e32 v7, v8, v7
	v_div_scale_f32 v8, vcc, v72, v5, v72
	v_mul_f32_e32 v9, v8, v7
	v_fma_f32 v10, -v6, v9, v8
	v_fmac_f32_e32 v9, v10, v7
	v_fma_f32 v6, -v6, v9, v8
	v_div_fmas_f32 v6, v6, v7, v9
	v_div_fixup_f32 v5, v6, v5, v72
	v_mul_f32_e32 v6, 0xbfb8aa3b, v76
	v_exp_f32_e32 v6, v6
	v_mul_f32_e32 v5, v56, v5
	v_add_f32_e32 v6, 1.0, v6
	v_div_scale_f32 v7, s[0:1], v6, v6, v76
	v_rcp_f32_e32 v8, v7
	s_nop 0
	v_fma_f32 v9, -v7, v8, 1.0
	v_fmac_f32_e32 v8, v9, v8
	v_div_scale_f32 v9, vcc, v76, v6, v76
	v_mul_f32_e32 v10, v9, v8
	v_fma_f32 v11, -v7, v10, v9
	v_fmac_f32_e32 v10, v11, v8
	v_fma_f32 v7, -v7, v10, v9
	v_div_fmas_f32 v7, v7, v8, v10
	v_div_fixup_f32 v6, v7, v6, v76
	v_mul_f32_e32 v7, 0xbfb8aa3b, v65
	v_exp_f32_e32 v7, v7
	v_mul_f32_e32 v6, v60, v6
	v_add_f32_e32 v7, 1.0, v7
	v_div_scale_f32 v8, s[0:1], v7, v7, v65
	v_rcp_f32_e32 v9, v8
	s_nop 0
	v_fma_f32 v10, -v8, v9, 1.0
	v_fmac_f32_e32 v9, v10, v9
	v_div_scale_f32 v10, vcc, v65, v7, v65
	v_mul_f32_e32 v11, v10, v9
	v_fma_f32 v12, -v8, v11, v10
	v_fmac_f32_e32 v11, v12, v9
	v_fma_f32 v8, -v8, v11, v10
	v_div_fmas_f32 v8, v8, v9, v11
	v_div_fixup_f32 v7, v8, v7, v65
	v_mul_f32_e32 v8, 0xbfb8aa3b, v69
	v_exp_f32_e32 v8, v8
	v_mul_f32_e32 v7, v49, v7
	v_add_f32_e32 v8, 1.0, v8
	v_div_scale_f32 v9, s[0:1], v8, v8, v69
	v_rcp_f32_e32 v10, v9
	s_nop 0
	v_fma_f32 v11, -v9, v10, 1.0
	v_fmac_f32_e32 v10, v11, v10
	v_div_scale_f32 v11, vcc, v69, v8, v69
	v_mul_f32_e32 v12, v11, v10
	v_fma_f32 v13, -v9, v12, v11
	v_fmac_f32_e32 v12, v13, v10
	v_fma_f32 v9, -v9, v12, v11
	v_div_fmas_f32 v9, v9, v10, v12
	v_div_fixup_f32 v8, v9, v8, v69
	v_mul_f32_e32 v9, 0xbfb8aa3b, v73
	v_exp_f32_e32 v9, v9
	v_mul_f32_e32 v8, v53, v8
	v_add_f32_e32 v9, 1.0, v9
	v_div_scale_f32 v10, s[0:1], v9, v9, v73
	v_rcp_f32_e32 v11, v10
	s_nop 0
	v_fma_f32 v12, -v10, v11, 1.0
	v_fmac_f32_e32 v11, v12, v11
	v_div_scale_f32 v12, vcc, v73, v9, v73
	v_mul_f32_e32 v13, v12, v11
	v_fma_f32 v14, -v10, v13, v12
	v_fmac_f32_e32 v13, v14, v11
	v_fma_f32 v10, -v10, v13, v12
	v_div_fmas_f32 v10, v10, v11, v13
	v_div_fixup_f32 v9, v10, v9, v73
	v_mul_f32_e32 v10, 0xbfb8aa3b, v77
	v_exp_f32_e32 v10, v10
	v_mul_f32_e32 v9, v57, v9
	v_add_f32_e32 v10, 1.0, v10
	v_div_scale_f32 v11, s[0:1], v10, v10, v77
	v_rcp_f32_e32 v12, v11
	s_nop 0
	v_fma_f32 v13, -v11, v12, 1.0
	v_fmac_f32_e32 v12, v13, v12
	v_div_scale_f32 v13, vcc, v77, v10, v77
	v_mul_f32_e32 v14, v13, v12
	v_fma_f32 v15, -v11, v14, v13
	v_fmac_f32_e32 v14, v15, v12
	v_fma_f32 v11, -v11, v14, v13
	v_div_fmas_f32 v11, v11, v12, v14
	v_div_fixup_f32 v10, v11, v10, v77
	v_mul_f32_e32 v11, 0xbfb8aa3b, v66
	v_exp_f32_e32 v11, v11
	v_mul_f32_e32 v10, v61, v10
	v_add_f32_e32 v11, 1.0, v11
	v_div_scale_f32 v12, s[0:1], v11, v11, v66
	v_rcp_f32_e32 v13, v12
	s_nop 0
	v_fma_f32 v14, -v12, v13, 1.0
	v_fmac_f32_e32 v13, v14, v13
	v_div_scale_f32 v14, vcc, v66, v11, v66
	v_mul_f32_e32 v15, v14, v13
	v_fma_f32 v48, -v12, v15, v14
	v_fmac_f32_e32 v15, v48, v13
	v_fma_f32 v12, -v12, v15, v14
	v_div_fmas_f32 v12, v12, v13, v15
	v_div_fixup_f32 v11, v12, v11, v66
	v_mul_f32_e32 v12, 0xbfb8aa3b, v70
	v_exp_f32_e32 v12, v12
	v_mul_f32_e32 v11, v50, v11
	v_add_f32_e32 v12, 1.0, v12
	v_div_scale_f32 v13, s[0:1], v12, v12, v70
	v_rcp_f32_e32 v14, v13
	s_nop 0
	v_fma_f32 v15, -v13, v14, 1.0
	v_fmac_f32_e32 v14, v15, v14
	v_div_scale_f32 v15, vcc, v70, v12, v70
	v_mul_f32_e32 v48, v15, v14
	v_fma_f32 v49, -v13, v48, v15
	v_fmac_f32_e32 v48, v49, v14
	v_fma_f32 v13, -v13, v48, v15
	v_div_fmas_f32 v13, v13, v14, v48
	v_div_fixup_f32 v12, v13, v12, v70
	v_mul_f32_e32 v15, v54, v12
	v_mul_f32_e32 v12, 0xbfb8aa3b, v74
	v_exp_f32_e32 v12, v12
	s_nop 0
	v_add_f32_e32 v12, 1.0, v12
	v_div_scale_f32 v13, s[0:1], v12, v12, v74
	v_rcp_f32_e32 v14, v13
	s_nop 0
	v_fma_f32 v48, -v13, v14, 1.0
	v_fmac_f32_e32 v14, v48, v14
	v_div_scale_f32 v48, vcc, v74, v12, v74
	v_mul_f32_e32 v49, v48, v14
	v_fma_f32 v50, -v13, v49, v48
	v_fmac_f32_e32 v49, v50, v14
	v_fma_f32 v13, -v13, v49, v48
	v_div_fmas_f32 v13, v13, v14, v49
	v_div_fixup_f32 v12, v13, v12, v74
	v_mul_f32_e32 v48, v58, v12
	v_mul_f32_e32 v12, 0xbfb8aa3b, v78
	v_exp_f32_e32 v12, v12
	s_nop 0
	v_add_f32_e32 v12, 1.0, v12
	v_div_scale_f32 v13, s[0:1], v12, v12, v78
	v_rcp_f32_e32 v14, v13
	s_nop 0
	v_fma_f32 v49, -v13, v14, 1.0
	v_fmac_f32_e32 v14, v49, v14
	v_div_scale_f32 v49, vcc, v78, v12, v78
	v_mul_f32_e32 v50, v49, v14
	v_fma_f32 v52, -v13, v50, v49
	v_fmac_f32_e32 v50, v52, v14
	v_fma_f32 v13, -v13, v50, v49
	v_div_fmas_f32 v13, v13, v14, v50
	v_div_fixup_f32 v12, v13, v12, v78
	v_mul_f32_e32 v49, v62, v12
	v_mul_f32_e32 v12, 0xbfb8aa3b, v67
	v_exp_f32_e32 v12, v12
	s_nop 0
	v_add_f32_e32 v12, 1.0, v12
	v_div_scale_f32 v13, s[0:1], v12, v12, v67
	v_rcp_f32_e32 v14, v13
	s_nop 0
	v_fma_f32 v50, -v13, v14, 1.0
	v_fmac_f32_e32 v14, v50, v14
	v_div_scale_f32 v50, vcc, v67, v12, v67
	v_mul_f32_e32 v52, v50, v14
	v_fma_f32 v53, -v13, v52, v50
	v_fmac_f32_e32 v52, v53, v14
	v_fma_f32 v13, -v13, v52, v50
	v_div_fmas_f32 v13, v13, v14, v52
	v_div_fixup_f32 v12, v13, v12, v67
	v_mul_f32_e32 v50, v51, v12
	v_mul_f32_e32 v12, 0xbfb8aa3b, v71
	v_exp_f32_e32 v12, v12
	s_nop 0
	v_add_f32_e32 v12, 1.0, v12
	v_div_scale_f32 v13, s[0:1], v12, v12, v71
	v_rcp_f32_e32 v14, v13
	s_nop 0
	v_fma_f32 v51, -v13, v14, 1.0
	v_fmac_f32_e32 v14, v51, v14
	v_div_scale_f32 v51, vcc, v71, v12, v71
	v_mul_f32_e32 v52, v51, v14
	v_fma_f32 v53, -v13, v52, v51
	v_fmac_f32_e32 v52, v53, v14
	v_fma_f32 v13, -v13, v52, v51
	v_div_fmas_f32 v13, v13, v14, v52
	v_div_fixup_f32 v12, v13, v12, v71
	v_mul_f32_e32 v51, v55, v12
	v_mul_f32_e32 v12, 0xbfb8aa3b, v75
	v_exp_f32_e32 v12, v12
	s_nop 0
	v_add_f32_e32 v12, 1.0, v12
	v_div_scale_f32 v13, s[0:1], v12, v12, v75
	v_rcp_f32_e32 v14, v13
	s_nop 0
	v_fma_f32 v52, -v13, v14, 1.0
	v_fmac_f32_e32 v14, v52, v14
	v_div_scale_f32 v52, vcc, v75, v12, v75
	v_mul_f32_e32 v53, v52, v14
	v_fma_f32 v54, -v13, v53, v52
	v_fmac_f32_e32 v53, v54, v14
	v_fma_f32 v13, -v13, v53, v52
	v_div_fmas_f32 v13, v13, v14, v53
	v_div_fixup_f32 v12, v13, v12, v75
	v_mul_f32_e32 v52, v59, v12
	v_mul_f32_e32 v12, 0xbfb8aa3b, v79
	v_exp_f32_e32 v12, v12
	s_nop 0
	v_add_f32_e32 v12, 1.0, v12
	v_div_scale_f32 v13, s[0:1], v12, v12, v79
	v_rcp_f32_e32 v14, v13
	s_nop 0
	v_fma_f32 v53, -v13, v14, 1.0
	v_fmac_f32_e32 v14, v53, v14
	v_div_scale_f32 v53, vcc, v79, v12, v79
	v_mul_f32_e32 v54, v53, v14
	v_fma_f32 v55, -v13, v54, v53
	v_fmac_f32_e32 v54, v55, v14
	v_fma_f32 v13, -v13, v54, v53
	v_div_fmas_f32 v13, v13, v14, v54
	v_div_fixup_f32 v12, v13, v12, v79
	v_mul_f32_e32 v53, v63, v12
	v_mov_b32_e32 v12, v1
	v_cvt_pk_fp8_f32 v12, v0, v4
	v_mul_f32_e32 v0, 0xbfb8aa3b, v32
	v_exp_f32_e32 v0, v0
	v_mov_b32_e32 v13, v1
	v_cvt_pk_fp8_f32 v12, v5, v6 op_sel:[0,0,1]
	v_cvt_pk_fp8_f32 v13, v7, v8
	v_add_f32_e32 v0, 1.0, v0
	v_div_scale_f32 v4, s[0:1], v0, v0, v32
	v_rcp_f32_e32 v5, v4
	v_cvt_pk_fp8_f32 v13, v9, v10 op_sel:[0,0,1]
	v_mov_b32_e32 v14, v1
	v_cvt_pk_fp8_f32 v14, v11, v15
	v_fma_f32 v6, -v4, v5, 1.0
	v_fmac_f32_e32 v5, v6, v5
	v_div_scale_f32 v6, vcc, v32, v0, v32
	v_mul_f32_e32 v7, v6, v5
	v_fma_f32 v8, -v4, v7, v6
	v_fmac_f32_e32 v7, v8, v5
	v_fma_f32 v4, -v4, v7, v6
	v_div_fmas_f32 v4, v4, v5, v7
	v_div_fixup_f32 v0, v4, v0, v32
	v_mul_f32_e32 v4, 0xbfb8aa3b, v36
	v_exp_f32_e32 v4, v4
	v_mov_b32_e32 v15, v1
	v_cvt_pk_fp8_f32 v15, v50, v51
	v_cvt_pk_fp8_f32 v14, v48, v49 op_sel:[0,0,1]
	v_add_f32_e32 v4, 1.0, v4
	v_div_scale_f32 v5, s[0:1], v4, v4, v36
	v_rcp_f32_e32 v6, v5
	v_cvt_pk_fp8_f32 v15, v52, v53 op_sel:[0,0,1]
	v_mul_f32_e32 v0, v16, v0
	v_fma_f32 v7, -v5, v6, 1.0
	v_fmac_f32_e32 v6, v7, v6
	v_div_scale_f32 v7, vcc, v36, v4, v36
	v_mul_f32_e32 v8, v7, v6
	v_fma_f32 v9, -v5, v8, v7
	v_fmac_f32_e32 v8, v9, v6
	v_fma_f32 v5, -v5, v8, v7
	v_div_fmas_f32 v5, v5, v6, v8
	v_div_fixup_f32 v4, v5, v4, v36
	v_mul_f32_e32 v5, 0xbfb8aa3b, v40
	v_exp_f32_e32 v5, v5
	global_store_dwordx4 v[2:3], v[12:15], off
	v_mul_f32_e32 v4, v20, v4
	v_add_f32_e32 v5, 1.0, v5
	v_div_scale_f32 v6, s[0:1], v5, v5, v40
	v_rcp_f32_e32 v7, v6
	s_nop 0
	v_fma_f32 v8, -v6, v7, 1.0
	v_fmac_f32_e32 v7, v8, v7
	v_div_scale_f32 v8, vcc, v40, v5, v40
	v_mul_f32_e32 v9, v8, v7
	v_fma_f32 v10, -v6, v9, v8
	v_fmac_f32_e32 v9, v10, v7
	v_fma_f32 v6, -v6, v9, v8
	v_div_fmas_f32 v6, v6, v7, v9
	v_div_fixup_f32 v5, v6, v5, v40
	v_mul_f32_e32 v6, 0xbfb8aa3b, v44
	v_exp_f32_e32 v6, v6
	v_mul_f32_e32 v5, v24, v5
	v_add_f32_e32 v6, 1.0, v6
	v_div_scale_f32 v7, s[0:1], v6, v6, v44
	v_rcp_f32_e32 v8, v7
	s_nop 0
	v_fma_f32 v9, -v7, v8, 1.0
	v_fmac_f32_e32 v8, v9, v8
	v_div_scale_f32 v9, vcc, v44, v6, v44
	v_mul_f32_e32 v10, v9, v8
	v_fma_f32 v11, -v7, v10, v9
	v_fmac_f32_e32 v10, v11, v8
	v_fma_f32 v7, -v7, v10, v9
	v_div_fmas_f32 v7, v7, v8, v10
	v_div_fixup_f32 v6, v7, v6, v44
	v_mul_f32_e32 v7, 0xbfb8aa3b, v33
	v_exp_f32_e32 v7, v7
	v_mul_f32_e32 v6, v28, v6
	v_add_f32_e32 v7, 1.0, v7
	v_div_scale_f32 v8, s[0:1], v7, v7, v33
	v_rcp_f32_e32 v9, v8
	s_nop 0
	v_fma_f32 v10, -v8, v9, 1.0
	v_fmac_f32_e32 v9, v10, v9
	v_div_scale_f32 v10, vcc, v33, v7, v33
	v_mul_f32_e32 v11, v10, v9
	v_fma_f32 v12, -v8, v11, v10
	v_fmac_f32_e32 v11, v12, v9
	v_fma_f32 v8, -v8, v11, v10
	v_div_fmas_f32 v8, v8, v9, v11
	v_div_fixup_f32 v7, v8, v7, v33
	v_mul_f32_e32 v8, 0xbfb8aa3b, v37
	v_exp_f32_e32 v8, v8
	v_mul_f32_e32 v7, v17, v7
	v_add_f32_e32 v8, 1.0, v8
	v_div_scale_f32 v9, s[0:1], v8, v8, v37
	v_rcp_f32_e32 v10, v9
	s_nop 0
	v_fma_f32 v11, -v9, v10, 1.0
	v_fmac_f32_e32 v10, v11, v10
	v_div_scale_f32 v11, vcc, v37, v8, v37
	v_mul_f32_e32 v12, v11, v10
	v_fma_f32 v13, -v9, v12, v11
	v_fmac_f32_e32 v12, v13, v10
	v_fma_f32 v9, -v9, v12, v11
	v_div_fmas_f32 v9, v9, v10, v12
	v_div_fixup_f32 v8, v9, v8, v37
	v_mul_f32_e32 v9, 0xbfb8aa3b, v41
	v_exp_f32_e32 v9, v9
	v_mul_f32_e32 v8, v21, v8
	v_add_f32_e32 v9, 1.0, v9
	v_div_scale_f32 v10, s[0:1], v9, v9, v41
	v_rcp_f32_e32 v11, v10
	s_nop 0
	v_fma_f32 v12, -v10, v11, 1.0
	v_fmac_f32_e32 v11, v12, v11
	v_div_scale_f32 v12, vcc, v41, v9, v41
	v_mul_f32_e32 v13, v12, v11
	v_fma_f32 v14, -v10, v13, v12
	v_fmac_f32_e32 v13, v14, v11
	v_fma_f32 v10, -v10, v13, v12
	v_div_fmas_f32 v10, v10, v11, v13
	v_div_fixup_f32 v9, v10, v9, v41
	v_mul_f32_e32 v10, 0xbfb8aa3b, v45
	v_exp_f32_e32 v10, v10
	v_mul_f32_e32 v9, v25, v9
	v_add_f32_e32 v10, 1.0, v10
	v_div_scale_f32 v11, s[0:1], v10, v10, v45
	v_rcp_f32_e32 v12, v11
	s_nop 0
	v_fma_f32 v13, -v11, v12, 1.0
	v_fmac_f32_e32 v12, v13, v12
	v_div_scale_f32 v13, vcc, v45, v10, v45
	v_mul_f32_e32 v14, v13, v12
	v_fma_f32 v15, -v11, v14, v13
	v_fmac_f32_e32 v14, v15, v12
	v_fma_f32 v11, -v11, v14, v13
	v_div_fmas_f32 v11, v11, v12, v14
	v_div_fixup_f32 v10, v11, v10, v45
	v_mul_f32_e32 v11, 0xbfb8aa3b, v34
	v_exp_f32_e32 v11, v11
	v_mul_f32_e32 v10, v29, v10
	v_add_f32_e32 v11, 1.0, v11
	v_div_scale_f32 v12, s[0:1], v11, v11, v34
	v_rcp_f32_e32 v13, v12
	s_nop 0
	v_fma_f32 v14, -v12, v13, 1.0
	v_fmac_f32_e32 v13, v14, v13
	v_div_scale_f32 v14, vcc, v34, v11, v34
	v_mul_f32_e32 v15, v14, v13
	v_fma_f32 v16, -v12, v15, v14
	v_fmac_f32_e32 v15, v16, v13
	v_fma_f32 v12, -v12, v15, v14
	v_div_fmas_f32 v12, v12, v13, v15
	v_div_fixup_f32 v11, v12, v11, v34
	v_mul_f32_e32 v12, 0xbfb8aa3b, v38
	v_exp_f32_e32 v12, v12
	v_mul_f32_e32 v11, v18, v11
	v_add_f32_e32 v12, 1.0, v12
	v_div_scale_f32 v13, s[0:1], v12, v12, v38
	v_rcp_f32_e32 v14, v13
	s_nop 0
	v_fma_f32 v15, -v13, v14, 1.0
	v_fmac_f32_e32 v14, v15, v14
	v_div_scale_f32 v15, vcc, v38, v12, v38
	v_mul_f32_e32 v16, v15, v14
	v_fma_f32 v17, -v13, v16, v15
	v_fmac_f32_e32 v16, v17, v14
	v_fma_f32 v13, -v13, v16, v15
	v_div_fmas_f32 v13, v13, v14, v16
	v_div_fixup_f32 v12, v13, v12, v38
	v_mul_f32_e32 v15, v22, v12
	v_mul_f32_e32 v12, 0xbfb8aa3b, v42
	v_exp_f32_e32 v12, v12
	s_nop 0
	v_add_f32_e32 v12, 1.0, v12
	v_div_scale_f32 v13, s[0:1], v12, v12, v42
	v_rcp_f32_e32 v14, v13
	s_nop 0
	v_fma_f32 v16, -v13, v14, 1.0
	v_fmac_f32_e32 v14, v16, v14
	v_div_scale_f32 v16, vcc, v42, v12, v42
	v_mul_f32_e32 v17, v16, v14
	v_fma_f32 v18, -v13, v17, v16
	v_fmac_f32_e32 v17, v18, v14
	v_fma_f32 v13, -v13, v17, v16
	v_div_fmas_f32 v13, v13, v14, v17
	v_div_fixup_f32 v12, v13, v12, v42
	v_mul_f32_e32 v16, v26, v12
	v_mul_f32_e32 v12, 0xbfb8aa3b, v46
	v_exp_f32_e32 v12, v12
	s_nop 0
	v_add_f32_e32 v12, 1.0, v12
	v_div_scale_f32 v13, s[0:1], v12, v12, v46
	v_rcp_f32_e32 v14, v13
	s_nop 0
	v_fma_f32 v17, -v13, v14, 1.0
	v_fmac_f32_e32 v14, v17, v14
	v_div_scale_f32 v17, vcc, v46, v12, v46
	v_mul_f32_e32 v18, v17, v14
	v_fma_f32 v20, -v13, v18, v17
	v_fmac_f32_e32 v18, v20, v14
	v_fma_f32 v13, -v13, v18, v17
	v_div_fmas_f32 v13, v13, v14, v18
	v_div_fixup_f32 v12, v13, v12, v46
	v_mul_f32_e32 v17, v30, v12
	v_mul_f32_e32 v12, 0xbfb8aa3b, v35
	v_exp_f32_e32 v12, v12
	s_nop 0
	v_add_f32_e32 v12, 1.0, v12
	v_div_scale_f32 v13, s[0:1], v12, v12, v35
	v_rcp_f32_e32 v14, v13
	s_nop 0
	v_fma_f32 v18, -v13, v14, 1.0
	v_fmac_f32_e32 v14, v18, v14
	v_div_scale_f32 v18, vcc, v35, v12, v35
	v_mul_f32_e32 v20, v18, v14
	v_fma_f32 v21, -v13, v20, v18
	v_fmac_f32_e32 v20, v21, v14
	v_fma_f32 v13, -v13, v20, v18
	v_div_fmas_f32 v13, v13, v14, v20
	v_div_fixup_f32 v12, v13, v12, v35
	v_mul_f32_e32 v18, v19, v12
	v_mul_f32_e32 v12, 0xbfb8aa3b, v39
	v_exp_f32_e32 v12, v12
	s_nop 0
	v_add_f32_e32 v12, 1.0, v12
	v_div_scale_f32 v13, s[0:1], v12, v12, v39
	v_rcp_f32_e32 v14, v13
	s_nop 0
	v_fma_f32 v19, -v13, v14, 1.0
	v_fmac_f32_e32 v14, v19, v14
	v_div_scale_f32 v19, vcc, v39, v12, v39
	v_mul_f32_e32 v20, v19, v14
	v_fma_f32 v21, -v13, v20, v19
	v_fmac_f32_e32 v20, v21, v14
	v_fma_f32 v13, -v13, v20, v19
	v_div_fmas_f32 v13, v13, v14, v20
	v_div_fixup_f32 v12, v13, v12, v39
	v_mul_f32_e32 v19, v23, v12
	v_mul_f32_e32 v12, 0xbfb8aa3b, v43
	v_exp_f32_e32 v12, v12
	s_nop 0
	v_add_f32_e32 v12, 1.0, v12
	v_div_scale_f32 v13, s[0:1], v12, v12, v43
	v_rcp_f32_e32 v14, v13
	s_nop 0
	v_fma_f32 v20, -v13, v14, 1.0
	v_fmac_f32_e32 v14, v20, v14
	v_div_scale_f32 v20, vcc, v43, v12, v43
	v_mul_f32_e32 v21, v20, v14
	v_fma_f32 v22, -v13, v21, v20
	v_fmac_f32_e32 v21, v22, v14
	v_fma_f32 v13, -v13, v21, v20
	v_div_fmas_f32 v13, v13, v14, v21
	v_div_fixup_f32 v12, v13, v12, v43
	v_mul_f32_e32 v20, v27, v12
	v_mul_f32_e32 v12, 0xbfb8aa3b, v47
	v_exp_f32_e32 v12, v12
	s_nop 0
	v_add_f32_e32 v12, 1.0, v12
	v_div_scale_f32 v13, s[0:1], v12, v12, v47
	v_rcp_f32_e32 v14, v13
	s_nop 0
	v_fma_f32 v21, -v13, v14, 1.0
	v_fmac_f32_e32 v14, v21, v14
	v_div_scale_f32 v21, vcc, v47, v12, v47
	v_mul_f32_e32 v22, v21, v14
	v_fma_f32 v23, -v13, v22, v21
	v_fmac_f32_e32 v22, v23, v14
	v_fma_f32 v13, -v13, v22, v21
	v_div_fmas_f32 v13, v13, v14, v22
	v_div_fixup_f32 v12, v13, v12, v47
	v_mov_b32_e32 v14, v1
	v_mul_f32_e32 v21, v31, v12
	v_mov_b32_e32 v12, v1
	v_mov_b32_e32 v13, v1
	v_cvt_pk_fp8_f32 v14, v11, v15
	v_mov_b32_e32 v15, v1
	v_cvt_pk_fp8_f32 v12, v0, v4
	v_cvt_pk_fp8_f32 v13, v7, v8
	v_cvt_pk_fp8_f32 v15, v18, v19
	v_cvt_pk_fp8_f32 v14, v16, v17 op_sel:[0,0,1]
	v_cvt_pk_fp8_f32 v12, v5, v6 op_sel:[0,0,1]
	v_cvt_pk_fp8_f32 v13, v9, v10 op_sel:[0,0,1]
	v_cvt_pk_fp8_f32 v15, v20, v21 op_sel:[0,0,1]
	global_store_dwordx4 v[2:3], v[12:15], off offset:32
	s_branch .LBB0_1322
